# v31 + fold-GEMM epilogue gain/scale hoist + layer-0 GEMM2 epilogue: x rows prefetched into dead residual registers with counted waits
# baseline (speedup 1.0000x reference)
.LBB0_745:
	s_ashr_i32 s24, s22, 2
	s_lshl_b32 s20, s24, 11
	s_ashr_i32 s21, s20, 31
	v_readlane_b32 s64, v251, 2
	s_lshl_b64 s[20:21], s[20:21], 2
	v_readlane_b32 s68, v251, 6
	v_lshl_or_b32 v154, s23, 8, v159
	v_readlane_b32 s69, v251, 7
	s_add_u32 s20, s68, s20
	s_addc_u32 s21, s69, s21
	v_ashrrev_i32_e32 v155, 31, v154
	s_lshl_b32 s13, s22, 8
	v_lshl_add_u64 v[152:153], v[154:155], 2, s[20:21]
	s_lshl_b32 s20, s24, 10
	s_and_b32 s13, s13, 0x300
	v_readlane_b32 s72, v251, 10
	v_readlane_b32 s73, v251, 11
	v_readlane_b32 s74, v251, 12
	v_readlane_b32 s75, v251, 13
	v_readlane_b32 s76, v251, 14
	v_readlane_b32 s77, v251, 15
	v_readlane_b32 s78, v251, 16
	v_readlane_b32 s79, v251, 17
	s_or_b32 s21, s20, s13
	v_add_u32_e32 v156, s21, v136
	v_readlane_b32 s72, v251, 38
	v_ashrrev_i32_e32 v157, 31, v156
	v_readlane_b32 s80, v251, 46
	v_readlane_b32 s81, v251, 47
	global_load_dwordx4 v[176:179], v[152:153], off
	global_load_dwordx4 v[180:183], v[152:153], off offset:16
	global_load_dwordx4 v[184:187], v[152:153], off offset:512
	global_load_dwordx4 v[188:191], v[152:153], off offset:528
	v_lshl_add_u64 v[156:157], v[156:157], 2, s[80:81]
	global_load_dword v192, v[156:157], off
	global_load_dword v193, v[156:157], off offset:64
	global_load_dword v194, v[156:157], off offset:128
	global_load_dword v195, v[156:157], off offset:192
	global_load_dword v196, v[156:157], off offset:512
	global_load_dword v197, v[156:157], off offset:576
	global_load_dword v198, v[156:157], off offset:640
	global_load_dword v199, v[156:157], off offset:704
	s_waitcnt vmcnt(0)
	s_nop 1
	v_mov_b64_e32 v[164:165], v[180:181]
	v_mov_b64_e32 v[166:167], v[182:183]
	s_nop 1
	v_mov_b64_e32 v[168:169], v[176:177]
	v_mov_b64_e32 v[170:171], v[178:179]
	v_mov_b32_e32 v172, v192
	s_mul_hi_i32 s21, s24, 0xc00
	s_mulk_i32 s24, 0xc00
	s_or_b32 s22, s24, s13
	s_add_u32 s22, s22, 0x800
	s_addc_u32 s23, s21, 0
	v_lshl_add_u64 v[174:175], s[22:23], 0, v[136:137]
	v_lshlrev_b64 v[174:175], 12, v[174:175]
	v_lshl_add_u64 v[174:175], s[4:5], 0, v[174:175]
	v_lshl_add_u64 v[174:175], v[154:155], 1, v[174:175]
	v_readlane_b32 s84, v251, 50
	v_readlane_b32 s85, v251, 51
	s_ashr_i32 s21, s20, 31
	v_readlane_b32 s65, v251, 3
	v_readlane_b32 s66, v251, 4
	v_readlane_b32 s67, v251, 5
	v_readlane_b32 s70, v251, 8
	v_readlane_b32 s71, v251, 9
	v_readlane_b32 s73, v251, 39
	v_readlane_b32 s74, v251, 40
	v_readlane_b32 s75, v251, 41
	v_readlane_b32 s76, v251, 42
	v_readlane_b32 s77, v251, 43
	v_readlane_b32 s78, v251, 44
	v_readlane_b32 s79, v251, 45
	v_readlane_b32 s82, v251, 48
	v_readlane_b32 s83, v251, 49
	v_readlane_b32 s86, v251, 52
	v_readlane_b32 s87, v251, 53
	v_pk_mul_f32 v[122:123], v[122:123], v[166:167]
	v_pk_mul_f32 v[120:121], v[120:121], v[164:165]
	v_pk_mul_f32 v[126:127], v[126:127], v[170:171]
	v_pk_mul_f32 v[124:125], v[124:125], v[168:169]
	v_pk_mul_f32 v[164:165], v[172:173], v[122:123] op_sel_hi:[0,1]
	v_pk_mul_f32 v[122:123], v[172:173], v[120:121] op_sel_hi:[0,1]
	v_pk_mul_f32 v[126:127], v[172:173], v[126:127] op_sel_hi:[0,1]
	v_pk_mul_f32 v[124:125], v[172:173], v[124:125] op_sel_hi:[0,1]
	v_cvt_pk_bf16_f32 v120, v124, v125
	v_cvt_pk_bf16_f32 v121, v126, v127
	v_cvt_pk_bf16_f32 v122, v122, v123
	v_cvt_pk_bf16_f32 v123, v164, v165
	global_store_dwordx4 v[174:175], v[120:123], off
	s_nop 1
	v_mov_b64_e32 v[124:125], v[184:185]
	v_mov_b64_e32 v[126:127], v[186:187]
	s_nop 1
	v_mov_b64_e32 v[164:165], v[188:189]
	v_mov_b64_e32 v[166:167], v[190:191]
	v_lshlrev_b32_e32 v170, 16, v123
	v_and_b32_e32 v123, 0xffff0000, v123
	v_lshlrev_b32_e32 v163, 16, v120
	v_and_b32_e32 v120, 0xffff0000, v120
	v_lshlrev_b32_e32 v168, 16, v121
	v_and_b32_e32 v121, 0xffff0000, v121
	v_max_f32_e64 v123, |v123|, |v123|
	v_max_f32_e64 v170, |v170|, |v170|
	v_lshlrev_b32_e32 v169, 16, v122
	v_and_b32_e32 v122, 0xffff0000, v122
	v_max_f32_e64 v120, |v120|, |v120|
	v_max_f32_e64 v163, |v163|, |v163|
	v_max_f32_e64 v121, |v121|, |v121|
	v_max_f32_e64 v168, |v168|, |v168|
	v_max_f32_e32 v123, v170, v123
	v_max_f32_e32 v120, v163, v120
	v_max_f32_e32 v121, v168, v121
	v_max3_f32 v122, |v169|, |v122|, v123
	v_max3_f32 v122, v120, v121, v122
	v_pk_mul_f32 v[118:119], v[118:119], v[126:127]
	v_pk_mul_f32 v[114:115], v[114:115], v[166:167]
	v_pk_mul_f32 v[112:113], v[112:113], v[164:165]
	v_pk_mul_f32 v[116:117], v[116:117], v[124:125]
	v_pk_mul_f32 v[120:121], v[172:173], v[114:115] op_sel_hi:[0,1]
	v_pk_mul_f32 v[114:115], v[172:173], v[112:113] op_sel_hi:[0,1]
	v_pk_mul_f32 v[118:119], v[172:173], v[118:119] op_sel_hi:[0,1]
	v_pk_mul_f32 v[116:117], v[172:173], v[116:117] op_sel_hi:[0,1]
	v_cvt_pk_bf16_f32 v112, v116, v117
	v_cvt_pk_bf16_f32 v113, v118, v119
	v_cvt_pk_bf16_f32 v114, v114, v115
	v_cvt_pk_bf16_f32 v115, v120, v121
	global_store_dwordx4 v[174:175], v[112:115], off offset:256
	v_lshlrev_b32_e32 v119, 16, v115
	v_lshlrev_b32_e32 v116, 16, v112
	v_and_b32_e32 v115, 0xffff0000, v115
	v_and_b32_e32 v112, 0xffff0000, v112
	v_lshlrev_b32_e32 v117, 16, v113
	v_and_b32_e32 v113, 0xffff0000, v113
	v_max_f32_e64 v115, |v115|, |v115|
	v_max_f32_e64 v119, |v119|, |v119|
	v_lshlrev_b32_e32 v118, 16, v114
	v_and_b32_e32 v114, 0xffff0000, v114
	v_max_f32_e64 v112, |v112|, |v112|
	v_max_f32_e64 v116, |v116|, |v116|
	v_max_f32_e64 v113, |v113|, |v113|
	v_max_f32_e64 v117, |v117|, |v117|
	v_max_f32_e32 v115, v119, v115
	v_max_f32_e32 v112, v116, v112
	v_max_f32_e32 v113, v117, v113
	v_max3_f32 v114, |v118|, |v114|, v115
	v_max3_f32 v112, v112, v113, v114
	v_max3_f32 v112, v122, 0, v112
	v_mov_b32_e32 v113, v112
	s_nop 1
	v_permlane16_swap_b32_e32 v112, v113
	v_max_f32_e32 v113, v113, v113
	v_max_f32_e32 v112, v112, v112
	v_max_f32_e32 v112, v112, v113
	v_mov_b32_e32 v113, v112
	s_nop 1
	v_permlane32_swap_b32_e32 v112, v113
	s_and_saveexec_b64 s[24:25], s[2:3]
	s_cbranch_execz .LBB0_747
	s_lshl_b64 s[26:27], s[20:21], 2
	s_add_u32 s26, s55, s26
	s_addc_u32 s27, s56, s27
	s_lshl_b32 s28, s13, 2
	s_add_u32 s26, s26, s28
	v_max_f32_e32 v112, v112, v112
	v_max_f32_e32 v113, v113, v113
	s_addc_u32 s27, s27, 0
	v_max_f32_e32 v114, v112, v113
	v_lshl_add_u64 v[112:113], v[136:137], 2, s[26:27]
	global_atomic_umax v[112:113], v114, off
.LBB0_747:
	s_or_b64 exec, exec, s[24:25]
	s_nop 1
	v_mov_b64_e32 v[112:113], v[176:177]
	v_mov_b64_e32 v[114:115], v[178:179]
	s_nop 1
	v_mov_b64_e32 v[116:117], v[180:181]
	v_mov_b64_e32 v[118:119], v[182:183]
	v_mov_b32_e32 v120, v193
	v_lshl_add_u64 v[122:123], s[22:23], 0, v[138:139]
	v_lshlrev_b64 v[122:123], 12, v[122:123]
	v_lshl_add_u64 v[122:123], s[4:5], 0, v[122:123]
	v_lshl_add_u64 v[122:123], v[154:155], 1, v[122:123]
	v_pk_mul_f32 v[110:111], v[110:111], v[114:115]
	v_pk_mul_f32 v[106:107], v[106:107], v[118:119]
	v_pk_mul_f32 v[104:105], v[104:105], v[116:117]
	v_pk_mul_f32 v[108:109], v[108:109], v[112:113]
	v_pk_mul_f32 v[112:113], v[120:121], v[106:107] op_sel_hi:[0,1]
	v_pk_mul_f32 v[106:107], v[120:121], v[104:105] op_sel_hi:[0,1]
	v_pk_mul_f32 v[110:111], v[120:121], v[110:111] op_sel_hi:[0,1]
	v_pk_mul_f32 v[108:109], v[120:121], v[108:109] op_sel_hi:[0,1]
	v_cvt_pk_bf16_f32 v104, v108, v109
	v_cvt_pk_bf16_f32 v105, v110, v111
	v_cvt_pk_bf16_f32 v106, v106, v107
	v_cvt_pk_bf16_f32 v107, v112, v113
	global_store_dwordx4 v[122:123], v[104:107], off
	s_nop 1
	v_mov_b64_e32 v[108:109], v[184:185]
	v_mov_b64_e32 v[110:111], v[186:187]
	s_nop 1
	v_mov_b64_e32 v[112:113], v[188:189]
	v_mov_b64_e32 v[114:115], v[190:191]
	v_lshlrev_b32_e32 v119, 16, v107
	v_and_b32_e32 v107, 0xffff0000, v107
	v_lshlrev_b32_e32 v116, 16, v104
	v_and_b32_e32 v104, 0xffff0000, v104
	v_lshlrev_b32_e32 v117, 16, v105
	v_and_b32_e32 v105, 0xffff0000, v105
	v_max_f32_e64 v107, |v107|, |v107|
	v_max_f32_e64 v119, |v119|, |v119|
	v_lshlrev_b32_e32 v118, 16, v106
	v_and_b32_e32 v106, 0xffff0000, v106
	v_max_f32_e64 v104, |v104|, |v104|
	v_max_f32_e64 v116, |v116|, |v116|
	v_max_f32_e64 v105, |v105|, |v105|
	v_max_f32_e64 v117, |v117|, |v117|
	v_max_f32_e32 v107, v119, v107
	v_max_f32_e32 v104, v116, v104
	v_max_f32_e32 v105, v117, v105
	v_max3_f32 v106, |v118|, |v106|, v107
	v_max3_f32 v106, v104, v105, v106
	v_pk_mul_f32 v[102:103], v[102:103], v[110:111]
	v_pk_mul_f32 v[98:99], v[98:99], v[114:115]
	v_pk_mul_f32 v[96:97], v[96:97], v[112:113]
	v_pk_mul_f32 v[100:101], v[100:101], v[108:109]
	v_pk_mul_f32 v[104:105], v[120:121], v[98:99] op_sel_hi:[0,1]
	v_pk_mul_f32 v[98:99], v[120:121], v[96:97] op_sel_hi:[0,1]
	v_pk_mul_f32 v[102:103], v[120:121], v[102:103] op_sel_hi:[0,1]
	v_pk_mul_f32 v[100:101], v[120:121], v[100:101] op_sel_hi:[0,1]
	v_cvt_pk_bf16_f32 v96, v100, v101
	v_cvt_pk_bf16_f32 v97, v102, v103
	v_cvt_pk_bf16_f32 v98, v98, v99
	v_cvt_pk_bf16_f32 v99, v104, v105
	global_store_dwordx4 v[122:123], v[96:99], off offset:256
	v_lshlrev_b32_e32 v103, 16, v99
	v_lshlrev_b32_e32 v100, 16, v96
	v_and_b32_e32 v99, 0xffff0000, v99
	v_and_b32_e32 v96, 0xffff0000, v96
	v_lshlrev_b32_e32 v101, 16, v97
	v_and_b32_e32 v97, 0xffff0000, v97
	v_max_f32_e64 v99, |v99|, |v99|
	v_max_f32_e64 v103, |v103|, |v103|
	v_lshlrev_b32_e32 v102, 16, v98
	v_and_b32_e32 v98, 0xffff0000, v98
	v_max_f32_e64 v96, |v96|, |v96|
	v_max_f32_e64 v100, |v100|, |v100|
	v_max_f32_e64 v97, |v97|, |v97|
	v_max_f32_e64 v101, |v101|, |v101|
	v_max_f32_e32 v99, v103, v99
	v_max_f32_e32 v96, v100, v96
	v_max_f32_e32 v97, v101, v97
	v_max3_f32 v98, |v102|, |v98|, v99
	v_max3_f32 v96, v96, v97, v98
	v_max3_f32 v96, v106, 0, v96
	v_mov_b32_e32 v97, v96
	s_nop 1
	v_permlane16_swap_b32_e32 v96, v97
	v_max_f32_e32 v97, v97, v97
	v_max_f32_e32 v96, v96, v96
	v_max_f32_e32 v96, v96, v97
	v_mov_b32_e32 v97, v96
	s_nop 1
	v_permlane32_swap_b32_e32 v96, v97
	s_and_saveexec_b64 s[24:25], s[2:3]
	s_cbranch_execz .LBB0_749
	s_lshl_b64 s[26:27], s[20:21], 2
	s_add_u32 s26, s55, s26
	s_addc_u32 s27, s56, s27
	s_lshl_b32 s28, s13, 2
	s_add_u32 s26, s26, s28
	v_max_f32_e32 v96, v96, v96
	v_max_f32_e32 v97, v97, v97
	s_addc_u32 s27, s27, 0
	v_max_f32_e32 v98, v96, v97
	v_lshl_add_u64 v[96:97], v[136:137], 2, s[26:27]
	global_atomic_umax v[96:97], v98, off offset:64
.LBB0_749:
	s_or_b64 exec, exec, s[24:25]
	s_nop 1
	v_mov_b64_e32 v[96:97], v[176:177]
	v_mov_b64_e32 v[98:99], v[178:179]
	s_nop 1
	v_mov_b64_e32 v[100:101], v[180:181]
	v_mov_b64_e32 v[102:103], v[182:183]
	v_mov_b32_e32 v104, v194
	v_lshl_add_u64 v[106:107], s[22:23], 0, v[140:141]
	v_lshlrev_b64 v[106:107], 12, v[106:107]
	v_lshl_add_u64 v[106:107], s[4:5], 0, v[106:107]
	v_lshl_add_u64 v[106:107], v[154:155], 1, v[106:107]
	v_pk_mul_f32 v[94:95], v[94:95], v[98:99]
	v_pk_mul_f32 v[90:91], v[90:91], v[102:103]
	v_pk_mul_f32 v[88:89], v[88:89], v[100:101]
	v_pk_mul_f32 v[92:93], v[92:93], v[96:97]
	v_pk_mul_f32 v[96:97], v[104:105], v[90:91] op_sel_hi:[0,1]
	v_pk_mul_f32 v[90:91], v[104:105], v[88:89] op_sel_hi:[0,1]
	v_pk_mul_f32 v[94:95], v[104:105], v[94:95] op_sel_hi:[0,1]
	v_pk_mul_f32 v[92:93], v[104:105], v[92:93] op_sel_hi:[0,1]
	v_cvt_pk_bf16_f32 v88, v92, v93
	v_cvt_pk_bf16_f32 v89, v94, v95
	v_cvt_pk_bf16_f32 v90, v90, v91
	v_cvt_pk_bf16_f32 v91, v96, v97
	global_store_dwordx4 v[106:107], v[88:91], off
	s_nop 1
	v_mov_b64_e32 v[92:93], v[184:185]
	v_mov_b64_e32 v[94:95], v[186:187]
	s_nop 1
	v_mov_b64_e32 v[96:97], v[188:189]
	v_mov_b64_e32 v[98:99], v[190:191]
	v_lshlrev_b32_e32 v103, 16, v91
	v_and_b32_e32 v91, 0xffff0000, v91
	v_lshlrev_b32_e32 v100, 16, v88
	v_and_b32_e32 v88, 0xffff0000, v88
	v_lshlrev_b32_e32 v101, 16, v89
	v_and_b32_e32 v89, 0xffff0000, v89
	v_max_f32_e64 v91, |v91|, |v91|
	v_max_f32_e64 v103, |v103|, |v103|
	v_lshlrev_b32_e32 v102, 16, v90
	v_and_b32_e32 v90, 0xffff0000, v90
	v_max_f32_e64 v88, |v88|, |v88|
	v_max_f32_e64 v100, |v100|, |v100|
	v_max_f32_e64 v89, |v89|, |v89|
	v_max_f32_e64 v101, |v101|, |v101|
	v_max_f32_e32 v91, v103, v91
	v_max_f32_e32 v88, v100, v88
	v_max_f32_e32 v89, v101, v89
	v_max3_f32 v90, |v102|, |v90|, v91
	v_max3_f32 v90, v88, v89, v90
	v_pk_mul_f32 v[86:87], v[86:87], v[94:95]
	v_pk_mul_f32 v[82:83], v[82:83], v[98:99]
	v_pk_mul_f32 v[80:81], v[80:81], v[96:97]
	v_pk_mul_f32 v[84:85], v[84:85], v[92:93]
	v_pk_mul_f32 v[88:89], v[104:105], v[82:83] op_sel_hi:[0,1]
	v_pk_mul_f32 v[82:83], v[104:105], v[80:81] op_sel_hi:[0,1]
	v_pk_mul_f32 v[86:87], v[104:105], v[86:87] op_sel_hi:[0,1]
	v_pk_mul_f32 v[84:85], v[104:105], v[84:85] op_sel_hi:[0,1]
	v_cvt_pk_bf16_f32 v80, v84, v85
	v_cvt_pk_bf16_f32 v81, v86, v87
	v_cvt_pk_bf16_f32 v82, v82, v83
	v_cvt_pk_bf16_f32 v83, v88, v89
	global_store_dwordx4 v[106:107], v[80:83], off offset:256
	v_lshlrev_b32_e32 v87, 16, v83
	v_lshlrev_b32_e32 v84, 16, v80
	v_and_b32_e32 v83, 0xffff0000, v83
	v_and_b32_e32 v80, 0xffff0000, v80
	v_lshlrev_b32_e32 v85, 16, v81
	v_and_b32_e32 v81, 0xffff0000, v81
	v_max_f32_e64 v83, |v83|, |v83|
	v_max_f32_e64 v87, |v87|, |v87|
	v_lshlrev_b32_e32 v86, 16, v82
	v_and_b32_e32 v82, 0xffff0000, v82
	v_max_f32_e64 v80, |v80|, |v80|
	v_max_f32_e64 v84, |v84|, |v84|
	v_max_f32_e64 v81, |v81|, |v81|
	v_max_f32_e64 v85, |v85|, |v85|
	v_max_f32_e32 v83, v87, v83
	v_max_f32_e32 v80, v84, v80
	v_max_f32_e32 v81, v85, v81
	v_max3_f32 v82, |v86|, |v82|, v83
	v_max3_f32 v80, v80, v81, v82
	v_max3_f32 v80, v90, 0, v80
	v_mov_b32_e32 v81, v80
	s_nop 1
	v_permlane16_swap_b32_e32 v80, v81
	v_max_f32_e32 v81, v81, v81
	v_max_f32_e32 v80, v80, v80
	v_max_f32_e32 v80, v80, v81
	v_mov_b32_e32 v81, v80
	s_nop 1
	v_permlane32_swap_b32_e32 v80, v81
	s_and_saveexec_b64 s[24:25], s[2:3]
	v_readlane_b32 s78, v251, 36
	v_readlane_b32 s70, v251, 58
	v_readlane_b32 s68, v251, 54
	v_readlane_b32 s69, v251, 55
	v_readlane_b32 s62, v251, 56
	v_readlane_b32 s79, v251, 37
	v_readlane_b32 s71, v251, 59
	s_cbranch_execz .LBB0_751
	s_lshl_b64 s[26:27], s[20:21], 2
	s_add_u32 s26, s55, s26
	s_addc_u32 s27, s56, s27
	s_lshl_b32 s28, s13, 2
	s_add_u32 s26, s26, s28
	v_max_f32_e32 v80, v80, v80
	v_max_f32_e32 v81, v81, v81
	s_addc_u32 s27, s27, 0
	v_max_f32_e32 v82, v80, v81
	v_lshl_add_u64 v[80:81], v[136:137], 2, s[26:27]
	global_atomic_umax v[80:81], v82, off offset:128
.LBB0_751:
	s_or_b64 exec, exec, s[24:25]
	s_nop 1
	v_mov_b64_e32 v[80:81], v[176:177]
	v_mov_b64_e32 v[82:83], v[178:179]
	s_nop 1
	v_mov_b64_e32 v[84:85], v[180:181]
	v_mov_b64_e32 v[86:87], v[182:183]
	v_mov_b32_e32 v88, v195
	v_lshl_add_u64 v[90:91], s[22:23], 0, v[142:143]
	v_lshlrev_b64 v[90:91], 12, v[90:91]
	v_lshl_add_u64 v[90:91], s[4:5], 0, v[90:91]
	v_lshl_add_u64 v[90:91], v[154:155], 1, v[90:91]
	v_pk_mul_f32 v[78:79], v[78:79], v[82:83]
	v_pk_mul_f32 v[74:75], v[74:75], v[86:87]
	v_pk_mul_f32 v[72:73], v[72:73], v[84:85]
	v_pk_mul_f32 v[76:77], v[76:77], v[80:81]
	v_pk_mul_f32 v[80:81], v[88:89], v[74:75] op_sel_hi:[0,1]
	v_pk_mul_f32 v[74:75], v[88:89], v[72:73] op_sel_hi:[0,1]
	v_pk_mul_f32 v[78:79], v[88:89], v[78:79] op_sel_hi:[0,1]
	v_pk_mul_f32 v[76:77], v[88:89], v[76:77] op_sel_hi:[0,1]
	v_cvt_pk_bf16_f32 v72, v76, v77
	v_cvt_pk_bf16_f32 v73, v78, v79
	v_cvt_pk_bf16_f32 v74, v74, v75
	v_cvt_pk_bf16_f32 v75, v80, v81
	global_store_dwordx4 v[90:91], v[72:75], off
	s_nop 1
	v_mov_b64_e32 v[76:77], v[184:185]
	v_mov_b64_e32 v[78:79], v[186:187]
	s_nop 1
	v_mov_b64_e32 v[80:81], v[188:189]
	v_mov_b64_e32 v[82:83], v[190:191]
	v_lshlrev_b32_e32 v87, 16, v75
	v_and_b32_e32 v75, 0xffff0000, v75
	v_lshlrev_b32_e32 v84, 16, v72
	v_and_b32_e32 v72, 0xffff0000, v72
	v_lshlrev_b32_e32 v85, 16, v73
	v_and_b32_e32 v73, 0xffff0000, v73
	v_max_f32_e64 v75, |v75|, |v75|
	v_max_f32_e64 v87, |v87|, |v87|
	v_lshlrev_b32_e32 v86, 16, v74
	v_and_b32_e32 v74, 0xffff0000, v74
	v_max_f32_e64 v72, |v72|, |v72|
	v_max_f32_e64 v84, |v84|, |v84|
	v_max_f32_e64 v73, |v73|, |v73|
	v_max_f32_e64 v85, |v85|, |v85|
	v_max_f32_e32 v75, v87, v75
	v_max_f32_e32 v72, v84, v72
	v_max_f32_e32 v73, v85, v73
	v_max3_f32 v74, |v86|, |v74|, v75
	v_max3_f32 v74, v72, v73, v74
	v_pk_mul_f32 v[70:71], v[70:71], v[78:79]
	v_pk_mul_f32 v[66:67], v[66:67], v[82:83]
	v_pk_mul_f32 v[64:65], v[64:65], v[80:81]
	v_pk_mul_f32 v[68:69], v[68:69], v[76:77]
	v_pk_mul_f32 v[72:73], v[88:89], v[66:67] op_sel_hi:[0,1]
	v_pk_mul_f32 v[66:67], v[88:89], v[64:65] op_sel_hi:[0,1]
	v_pk_mul_f32 v[70:71], v[88:89], v[70:71] op_sel_hi:[0,1]
	v_pk_mul_f32 v[68:69], v[88:89], v[68:69] op_sel_hi:[0,1]
	v_cvt_pk_bf16_f32 v64, v68, v69
	v_cvt_pk_bf16_f32 v65, v70, v71
	v_cvt_pk_bf16_f32 v66, v66, v67
	v_cvt_pk_bf16_f32 v67, v72, v73
	global_store_dwordx4 v[90:91], v[64:67], off offset:256
	v_lshlrev_b32_e32 v71, 16, v67
	v_lshlrev_b32_e32 v68, 16, v64
	v_and_b32_e32 v67, 0xffff0000, v67
	v_and_b32_e32 v64, 0xffff0000, v64
	v_lshlrev_b32_e32 v69, 16, v65
	v_and_b32_e32 v65, 0xffff0000, v65
	v_max_f32_e64 v67, |v67|, |v67|
	v_max_f32_e64 v71, |v71|, |v71|
	v_lshlrev_b32_e32 v70, 16, v66
	v_and_b32_e32 v66, 0xffff0000, v66
	v_max_f32_e64 v64, |v64|, |v64|
	v_max_f32_e64 v68, |v68|, |v68|
	v_max_f32_e64 v65, |v65|, |v65|
	v_max_f32_e64 v69, |v69|, |v69|
	v_max_f32_e32 v67, v71, v67
	v_max_f32_e32 v64, v68, v64
	v_max_f32_e32 v65, v69, v65
	v_max3_f32 v66, |v70|, |v66|, v67
	v_max3_f32 v64, v64, v65, v66
	v_max3_f32 v64, v74, 0, v64
	v_mov_b32_e32 v65, v64
	s_nop 1
	v_permlane16_swap_b32_e32 v64, v65
	v_max_f32_e32 v65, v65, v65
	v_max_f32_e32 v64, v64, v64
	v_max_f32_e32 v64, v64, v65
	v_mov_b32_e32 v65, v64
	s_nop 1
	v_permlane32_swap_b32_e32 v64, v65
	s_and_saveexec_b64 s[24:25], s[2:3]
	s_cbranch_execz .LBB0_753
	s_lshl_b64 s[26:27], s[20:21], 2
	s_add_u32 s26, s55, s26
	s_addc_u32 s27, s56, s27
	s_lshl_b32 s28, s13, 2
	s_add_u32 s26, s26, s28
	v_max_f32_e32 v64, v64, v64
	v_max_f32_e32 v65, v65, v65
	s_addc_u32 s27, s27, 0
	v_max_f32_e32 v66, v64, v65
	v_lshl_add_u64 v[64:65], v[136:137], 2, s[26:27]
	global_atomic_umax v[64:65], v66, off offset:192
.LBB0_753:
	s_or_b64 exec, exec, s[24:25]
	s_nop 1
	v_mov_b64_e32 v[64:65], v[176:177]
	v_mov_b64_e32 v[66:67], v[178:179]
	s_nop 1
	v_mov_b64_e32 v[68:69], v[180:181]
	v_mov_b64_e32 v[70:71], v[182:183]
	v_mov_b32_e32 v72, v196
	v_lshl_add_u64 v[74:75], s[22:23], 0, v[144:145]
	v_lshlrev_b64 v[74:75], 12, v[74:75]
	v_lshl_add_u64 v[74:75], s[4:5], 0, v[74:75]
	v_lshl_add_u64 v[74:75], v[154:155], 1, v[74:75]
	v_pk_mul_f32 v[62:63], v[62:63], v[66:67]
	v_pk_mul_f32 v[58:59], v[58:59], v[70:71]
	v_pk_mul_f32 v[56:57], v[56:57], v[68:69]
	v_pk_mul_f32 v[60:61], v[60:61], v[64:65]
	v_pk_mul_f32 v[64:65], v[72:73], v[58:59] op_sel_hi:[0,1]
	v_pk_mul_f32 v[58:59], v[72:73], v[56:57] op_sel_hi:[0,1]
	v_pk_mul_f32 v[62:63], v[72:73], v[62:63] op_sel_hi:[0,1]
	v_pk_mul_f32 v[60:61], v[72:73], v[60:61] op_sel_hi:[0,1]
	v_cvt_pk_bf16_f32 v56, v60, v61
	v_cvt_pk_bf16_f32 v57, v62, v63
	v_cvt_pk_bf16_f32 v58, v58, v59
	v_cvt_pk_bf16_f32 v59, v64, v65
	global_store_dwordx4 v[74:75], v[56:59], off
	s_nop 1
	v_mov_b64_e32 v[60:61], v[184:185]
	v_mov_b64_e32 v[62:63], v[186:187]
	s_nop 1
	v_mov_b64_e32 v[64:65], v[188:189]
	v_mov_b64_e32 v[66:67], v[190:191]
	v_lshlrev_b32_e32 v71, 16, v59
	v_and_b32_e32 v59, 0xffff0000, v59
	v_lshlrev_b32_e32 v68, 16, v56
	v_and_b32_e32 v56, 0xffff0000, v56
	v_lshlrev_b32_e32 v69, 16, v57
	v_and_b32_e32 v57, 0xffff0000, v57
	v_max_f32_e64 v59, |v59|, |v59|
	v_max_f32_e64 v71, |v71|, |v71|
	v_lshlrev_b32_e32 v70, 16, v58
	v_and_b32_e32 v58, 0xffff0000, v58
	v_max_f32_e64 v56, |v56|, |v56|
	v_max_f32_e64 v68, |v68|, |v68|
	v_max_f32_e64 v57, |v57|, |v57|
	v_max_f32_e64 v69, |v69|, |v69|
	v_max_f32_e32 v59, v71, v59
	v_max_f32_e32 v56, v68, v56
	v_max_f32_e32 v57, v69, v57
	v_max3_f32 v58, |v70|, |v58|, v59
	v_max3_f32 v58, v56, v57, v58
	v_pk_mul_f32 v[54:55], v[54:55], v[62:63]
	v_pk_mul_f32 v[50:51], v[50:51], v[66:67]
	v_pk_mul_f32 v[48:49], v[48:49], v[64:65]
	v_pk_mul_f32 v[52:53], v[52:53], v[60:61]
	v_pk_mul_f32 v[56:57], v[72:73], v[50:51] op_sel_hi:[0,1]
	v_pk_mul_f32 v[50:51], v[72:73], v[48:49] op_sel_hi:[0,1]
	v_pk_mul_f32 v[54:55], v[72:73], v[54:55] op_sel_hi:[0,1]
	v_pk_mul_f32 v[52:53], v[72:73], v[52:53] op_sel_hi:[0,1]
	v_cvt_pk_bf16_f32 v48, v52, v53
	v_cvt_pk_bf16_f32 v49, v54, v55
	v_cvt_pk_bf16_f32 v50, v50, v51
	v_cvt_pk_bf16_f32 v51, v56, v57
	global_store_dwordx4 v[74:75], v[48:51], off offset:256
	v_lshlrev_b32_e32 v55, 16, v51
	v_lshlrev_b32_e32 v52, 16, v48
	v_and_b32_e32 v51, 0xffff0000, v51
	v_and_b32_e32 v48, 0xffff0000, v48
	v_lshlrev_b32_e32 v53, 16, v49
	v_and_b32_e32 v49, 0xffff0000, v49
	v_max_f32_e64 v51, |v51|, |v51|
	v_max_f32_e64 v55, |v55|, |v55|
	v_lshlrev_b32_e32 v54, 16, v50
	v_and_b32_e32 v50, 0xffff0000, v50
	v_max_f32_e64 v48, |v48|, |v48|
	v_max_f32_e64 v52, |v52|, |v52|
	v_max_f32_e64 v49, |v49|, |v49|
	v_max_f32_e64 v53, |v53|, |v53|
	v_max_f32_e32 v51, v55, v51
	v_max_f32_e32 v48, v52, v48
	v_max_f32_e32 v49, v53, v49
	v_max3_f32 v50, |v54|, |v50|, v51
	v_max3_f32 v48, v48, v49, v50
	v_max3_f32 v48, v58, 0, v48
	v_mov_b32_e32 v49, v48
	s_nop 1
	v_permlane16_swap_b32_e32 v48, v49
	v_max_f32_e32 v49, v49, v49
	v_max_f32_e32 v48, v48, v48
	v_max_f32_e32 v48, v48, v49
	v_mov_b32_e32 v49, v48
	s_nop 1
	v_permlane32_swap_b32_e32 v48, v49
	s_and_saveexec_b64 s[24:25], s[2:3]
	s_cbranch_execz .LBB0_755
	s_lshl_b64 s[26:27], s[20:21], 2
	s_add_u32 s26, s55, s26
	s_addc_u32 s27, s56, s27
	s_lshl_b32 s28, s13, 2
	s_add_u32 s26, s26, s28
	v_max_f32_e32 v48, v48, v48
	v_max_f32_e32 v49, v49, v49
	s_addc_u32 s27, s27, 0
	v_max_f32_e32 v50, v48, v49
	v_lshl_add_u64 v[48:49], v[136:137], 2, s[26:27]
	global_atomic_umax v[48:49], v50, off offset:512
.LBB0_755:
	s_or_b64 exec, exec, s[24:25]
	s_nop 1
	v_mov_b64_e32 v[48:49], v[176:177]
	v_mov_b64_e32 v[50:51], v[178:179]
	s_nop 1
	v_mov_b64_e32 v[52:53], v[180:181]
	v_mov_b64_e32 v[54:55], v[182:183]
	v_mov_b32_e32 v56, v197
	v_lshl_add_u64 v[58:59], s[22:23], 0, v[146:147]
	v_lshlrev_b64 v[58:59], 12, v[58:59]
	v_lshl_add_u64 v[58:59], s[4:5], 0, v[58:59]
	v_lshl_add_u64 v[58:59], v[154:155], 1, v[58:59]
	v_pk_mul_f32 v[46:47], v[46:47], v[50:51]
	v_pk_mul_f32 v[42:43], v[42:43], v[54:55]
	v_pk_mul_f32 v[40:41], v[40:41], v[52:53]
	v_pk_mul_f32 v[44:45], v[44:45], v[48:49]
	v_pk_mul_f32 v[48:49], v[56:57], v[42:43] op_sel_hi:[0,1]
	v_pk_mul_f32 v[42:43], v[56:57], v[40:41] op_sel_hi:[0,1]
	v_pk_mul_f32 v[46:47], v[56:57], v[46:47] op_sel_hi:[0,1]
	v_pk_mul_f32 v[44:45], v[56:57], v[44:45] op_sel_hi:[0,1]
	v_cvt_pk_bf16_f32 v40, v44, v45
	v_cvt_pk_bf16_f32 v41, v46, v47
	v_cvt_pk_bf16_f32 v42, v42, v43
	v_cvt_pk_bf16_f32 v43, v48, v49
	global_store_dwordx4 v[58:59], v[40:43], off
	s_nop 1
	v_mov_b64_e32 v[44:45], v[184:185]
	v_mov_b64_e32 v[46:47], v[186:187]
	s_nop 1
	v_mov_b64_e32 v[48:49], v[188:189]
	v_mov_b64_e32 v[50:51], v[190:191]
	v_lshlrev_b32_e32 v55, 16, v43
	v_and_b32_e32 v43, 0xffff0000, v43
	v_lshlrev_b32_e32 v52, 16, v40
	v_and_b32_e32 v40, 0xffff0000, v40
	v_lshlrev_b32_e32 v53, 16, v41
	v_and_b32_e32 v41, 0xffff0000, v41
	v_max_f32_e64 v43, |v43|, |v43|
	v_max_f32_e64 v55, |v55|, |v55|
	v_lshlrev_b32_e32 v54, 16, v42
	v_and_b32_e32 v42, 0xffff0000, v42
	v_max_f32_e64 v40, |v40|, |v40|
	v_max_f32_e64 v52, |v52|, |v52|
	v_max_f32_e64 v41, |v41|, |v41|
	v_max_f32_e64 v53, |v53|, |v53|
	v_max_f32_e32 v43, v55, v43
	v_max_f32_e32 v40, v52, v40
	v_max_f32_e32 v41, v53, v41
	v_max3_f32 v42, |v54|, |v42|, v43
	v_max3_f32 v42, v40, v41, v42
	v_pk_mul_f32 v[38:39], v[38:39], v[46:47]
	v_pk_mul_f32 v[34:35], v[34:35], v[50:51]
	v_pk_mul_f32 v[32:33], v[32:33], v[48:49]
	v_pk_mul_f32 v[36:37], v[36:37], v[44:45]
	v_pk_mul_f32 v[40:41], v[56:57], v[34:35] op_sel_hi:[0,1]
	v_pk_mul_f32 v[34:35], v[56:57], v[32:33] op_sel_hi:[0,1]
	v_pk_mul_f32 v[38:39], v[56:57], v[38:39] op_sel_hi:[0,1]
	v_pk_mul_f32 v[36:37], v[56:57], v[36:37] op_sel_hi:[0,1]
	v_cvt_pk_bf16_f32 v32, v36, v37
	v_cvt_pk_bf16_f32 v33, v38, v39
	v_cvt_pk_bf16_f32 v34, v34, v35
	v_cvt_pk_bf16_f32 v35, v40, v41
	global_store_dwordx4 v[58:59], v[32:35], off offset:256
	v_lshlrev_b32_e32 v39, 16, v35
	v_lshlrev_b32_e32 v36, 16, v32
	v_and_b32_e32 v35, 0xffff0000, v35
	v_and_b32_e32 v32, 0xffff0000, v32
	v_lshlrev_b32_e32 v37, 16, v33
	v_and_b32_e32 v33, 0xffff0000, v33
	v_max_f32_e64 v35, |v35|, |v35|
	v_max_f32_e64 v39, |v39|, |v39|
	v_lshlrev_b32_e32 v38, 16, v34
	v_and_b32_e32 v34, 0xffff0000, v34
	v_max_f32_e64 v32, |v32|, |v32|
	v_max_f32_e64 v36, |v36|, |v36|
	v_max_f32_e64 v33, |v33|, |v33|
	v_max_f32_e64 v37, |v37|, |v37|
	v_max_f32_e32 v35, v39, v35
	v_max_f32_e32 v32, v36, v32
	v_max_f32_e32 v33, v37, v33
	v_max3_f32 v34, |v38|, |v34|, v35
	v_max3_f32 v32, v32, v33, v34
	v_max3_f32 v32, v42, 0, v32
	v_mov_b32_e32 v33, v32
	s_nop 1
	v_permlane16_swap_b32_e32 v32, v33
	v_max_f32_e32 v33, v33, v33
	v_max_f32_e32 v32, v32, v32
	v_max_f32_e32 v32, v32, v33
	v_mov_b32_e32 v33, v32
	s_nop 1
	v_permlane32_swap_b32_e32 v32, v33
	s_and_saveexec_b64 s[24:25], s[2:3]
	s_cbranch_execz .LBB0_757
	s_lshl_b64 s[26:27], s[20:21], 2
	s_add_u32 s26, s55, s26
	s_addc_u32 s27, s56, s27
	s_lshl_b32 s28, s13, 2
	s_add_u32 s26, s26, s28
	v_max_f32_e32 v32, v32, v32
	v_max_f32_e32 v33, v33, v33
	s_addc_u32 s27, s27, 0
	v_max_f32_e32 v34, v32, v33
	v_lshl_add_u64 v[32:33], v[136:137], 2, s[26:27]
	global_atomic_umax v[32:33], v34, off offset:576
.LBB0_757:
	s_or_b64 exec, exec, s[24:25]
	s_nop 1
	v_mov_b64_e32 v[32:33], v[176:177]
	v_mov_b64_e32 v[34:35], v[178:179]
	s_nop 1
	v_mov_b64_e32 v[36:37], v[180:181]
	v_mov_b64_e32 v[38:39], v[182:183]
	v_mov_b32_e32 v40, v198
	v_lshl_add_u64 v[42:43], s[22:23], 0, v[148:149]
	v_lshlrev_b64 v[42:43], 12, v[42:43]
	v_lshl_add_u64 v[42:43], s[4:5], 0, v[42:43]
	v_lshl_add_u64 v[42:43], v[154:155], 1, v[42:43]
	v_pk_mul_f32 v[30:31], v[30:31], v[34:35]
	v_pk_mul_f32 v[26:27], v[26:27], v[38:39]
	v_pk_mul_f32 v[24:25], v[24:25], v[36:37]
	v_pk_mul_f32 v[28:29], v[28:29], v[32:33]
	v_pk_mul_f32 v[32:33], v[40:41], v[26:27] op_sel_hi:[0,1]
	v_pk_mul_f32 v[26:27], v[40:41], v[24:25] op_sel_hi:[0,1]
	v_pk_mul_f32 v[30:31], v[40:41], v[30:31] op_sel_hi:[0,1]
	v_pk_mul_f32 v[28:29], v[40:41], v[28:29] op_sel_hi:[0,1]
	v_cvt_pk_bf16_f32 v24, v28, v29
	v_cvt_pk_bf16_f32 v25, v30, v31
	v_cvt_pk_bf16_f32 v26, v26, v27
	v_cvt_pk_bf16_f32 v27, v32, v33
	global_store_dwordx4 v[42:43], v[24:27], off
	s_nop 1
	v_mov_b64_e32 v[28:29], v[184:185]
	v_mov_b64_e32 v[30:31], v[186:187]
	s_nop 1
	v_mov_b64_e32 v[32:33], v[188:189]
	v_mov_b64_e32 v[34:35], v[190:191]
	v_lshlrev_b32_e32 v39, 16, v27
	v_and_b32_e32 v27, 0xffff0000, v27
	v_lshlrev_b32_e32 v36, 16, v24
	v_and_b32_e32 v24, 0xffff0000, v24
	v_lshlrev_b32_e32 v37, 16, v25
	v_and_b32_e32 v25, 0xffff0000, v25
	v_max_f32_e64 v27, |v27|, |v27|
	v_max_f32_e64 v39, |v39|, |v39|
	v_lshlrev_b32_e32 v38, 16, v26
	v_and_b32_e32 v26, 0xffff0000, v26
	v_max_f32_e64 v24, |v24|, |v24|
	v_max_f32_e64 v36, |v36|, |v36|
	v_max_f32_e64 v25, |v25|, |v25|
	v_max_f32_e64 v37, |v37|, |v37|
	v_max_f32_e32 v27, v39, v27
	v_max_f32_e32 v24, v36, v24
	v_max_f32_e32 v25, v37, v25
	v_max3_f32 v26, |v38|, |v26|, v27
	v_max3_f32 v26, v24, v25, v26
	v_pk_mul_f32 v[22:23], v[22:23], v[30:31]
	v_pk_mul_f32 v[18:19], v[18:19], v[34:35]
	v_pk_mul_f32 v[16:17], v[16:17], v[32:33]
	v_pk_mul_f32 v[20:21], v[20:21], v[28:29]
	v_pk_mul_f32 v[24:25], v[40:41], v[18:19] op_sel_hi:[0,1]
	v_pk_mul_f32 v[18:19], v[40:41], v[16:17] op_sel_hi:[0,1]
	v_pk_mul_f32 v[22:23], v[40:41], v[22:23] op_sel_hi:[0,1]
	v_pk_mul_f32 v[20:21], v[40:41], v[20:21] op_sel_hi:[0,1]
	v_cvt_pk_bf16_f32 v16, v20, v21
	v_cvt_pk_bf16_f32 v17, v22, v23
	v_cvt_pk_bf16_f32 v18, v18, v19
	v_cvt_pk_bf16_f32 v19, v24, v25
	global_store_dwordx4 v[42:43], v[16:19], off offset:256
	v_lshlrev_b32_e32 v23, 16, v19
	v_lshlrev_b32_e32 v20, 16, v16
	v_and_b32_e32 v19, 0xffff0000, v19
	v_and_b32_e32 v16, 0xffff0000, v16
	v_lshlrev_b32_e32 v21, 16, v17
	v_and_b32_e32 v17, 0xffff0000, v17
	v_max_f32_e64 v19, |v19|, |v19|
	v_max_f32_e64 v23, |v23|, |v23|
	v_lshlrev_b32_e32 v22, 16, v18
	v_and_b32_e32 v18, 0xffff0000, v18
	v_max_f32_e64 v16, |v16|, |v16|
	v_max_f32_e64 v20, |v20|, |v20|
	v_max_f32_e64 v17, |v17|, |v17|
	v_max_f32_e64 v21, |v21|, |v21|
	v_max_f32_e32 v19, v23, v19
	v_max_f32_e32 v16, v20, v16
	v_max_f32_e32 v17, v21, v17
	v_max3_f32 v18, |v22|, |v18|, v19
	v_max3_f32 v16, v16, v17, v18
	v_max3_f32 v16, v26, 0, v16
	v_mov_b32_e32 v17, v16
	s_nop 1
	v_permlane16_swap_b32_e32 v16, v17
	v_max_f32_e32 v17, v17, v17
	v_max_f32_e32 v16, v16, v16
	v_max_f32_e32 v16, v16, v17
	v_mov_b32_e32 v17, v16
	s_nop 1
	v_permlane32_swap_b32_e32 v16, v17
	s_and_saveexec_b64 s[24:25], s[2:3]
	s_cbranch_execz .LBB0_759
	s_lshl_b64 s[26:27], s[20:21], 2
	s_add_u32 s26, s55, s26
	s_addc_u32 s27, s56, s27
	s_lshl_b32 s28, s13, 2
	s_add_u32 s26, s26, s28
	v_max_f32_e32 v16, v16, v16
	v_max_f32_e32 v17, v17, v17
	s_addc_u32 s27, s27, 0
	v_max_f32_e32 v18, v16, v17
	v_lshl_add_u64 v[16:17], v[136:137], 2, s[26:27]
	global_atomic_umax v[16:17], v18, off offset:640
.LBB0_759:
	s_or_b64 exec, exec, s[24:25]
	s_nop 1
	v_mov_b64_e32 v[16:17], v[176:177]
	v_mov_b64_e32 v[18:19], v[178:179]
	s_nop 1
	v_mov_b64_e32 v[20:21], v[180:181]
	v_mov_b64_e32 v[22:23], v[182:183]
	v_mov_b32_e32 v24, v199
	v_lshl_add_u64 v[26:27], s[22:23], 0, v[150:151]
	v_lshlrev_b64 v[26:27], 12, v[26:27]
	v_lshl_add_u64 v[26:27], s[4:5], 0, v[26:27]
	v_lshl_add_u64 v[26:27], v[154:155], 1, v[26:27]
	v_pk_mul_f32 v[14:15], v[14:15], v[18:19]
	v_pk_mul_f32 v[10:11], v[10:11], v[22:23]
	v_pk_mul_f32 v[8:9], v[8:9], v[20:21]
	v_pk_mul_f32 v[12:13], v[12:13], v[16:17]
	v_pk_mul_f32 v[16:17], v[24:25], v[10:11] op_sel_hi:[0,1]
	v_pk_mul_f32 v[10:11], v[24:25], v[8:9] op_sel_hi:[0,1]
	v_pk_mul_f32 v[14:15], v[24:25], v[14:15] op_sel_hi:[0,1]
	v_pk_mul_f32 v[12:13], v[24:25], v[12:13] op_sel_hi:[0,1]
	v_cvt_pk_bf16_f32 v8, v12, v13
	v_cvt_pk_bf16_f32 v9, v14, v15
	v_cvt_pk_bf16_f32 v10, v10, v11
	v_cvt_pk_bf16_f32 v11, v16, v17
	global_store_dwordx4 v[26:27], v[8:11], off
	s_nop 1
	v_mov_b64_e32 v[12:13], v[184:185]
	v_mov_b64_e32 v[14:15], v[186:187]
	s_nop 1
	v_mov_b64_e32 v[16:17], v[188:189]
	v_mov_b64_e32 v[18:19], v[190:191]
	v_lshlrev_b32_e32 v23, 16, v11
	v_and_b32_e32 v11, 0xffff0000, v11
	v_lshlrev_b32_e32 v20, 16, v8
	v_and_b32_e32 v8, 0xffff0000, v8
	v_lshlrev_b32_e32 v21, 16, v9
	v_and_b32_e32 v9, 0xffff0000, v9
	v_max_f32_e64 v11, |v11|, |v11|
	v_max_f32_e64 v23, |v23|, |v23|
	v_lshlrev_b32_e32 v22, 16, v10
	v_and_b32_e32 v10, 0xffff0000, v10
	v_max_f32_e64 v8, |v8|, |v8|
	v_max_f32_e64 v20, |v20|, |v20|
	v_max_f32_e64 v9, |v9|, |v9|
	v_max_f32_e64 v21, |v21|, |v21|
	v_max_f32_e32 v11, v23, v11
	v_max_f32_e32 v8, v20, v8
	v_max_f32_e32 v9, v21, v9
	v_max3_f32 v10, |v22|, |v10|, v11
	v_max3_f32 v10, v8, v9, v10
	v_pk_mul_f32 v[6:7], v[6:7], v[14:15]
	v_pk_mul_f32 v[2:3], v[2:3], v[18:19]
	v_pk_mul_f32 v[0:1], v[0:1], v[16:17]
	v_pk_mul_f32 v[4:5], v[4:5], v[12:13]
	v_pk_mul_f32 v[8:9], v[24:25], v[2:3] op_sel_hi:[0,1]
	v_pk_mul_f32 v[2:3], v[24:25], v[0:1] op_sel_hi:[0,1]
	v_pk_mul_f32 v[6:7], v[24:25], v[6:7] op_sel_hi:[0,1]
	v_pk_mul_f32 v[4:5], v[24:25], v[4:5] op_sel_hi:[0,1]
	v_cvt_pk_bf16_f32 v0, v4, v5
	v_cvt_pk_bf16_f32 v1, v6, v7
	v_cvt_pk_bf16_f32 v2, v2, v3
	v_cvt_pk_bf16_f32 v3, v8, v9
	global_store_dwordx4 v[26:27], v[0:3], off offset:256
	v_lshlrev_b32_e32 v7, 16, v3
	v_lshlrev_b32_e32 v4, 16, v0
	v_and_b32_e32 v3, 0xffff0000, v3
	v_and_b32_e32 v0, 0xffff0000, v0
	v_lshlrev_b32_e32 v5, 16, v1
	v_and_b32_e32 v1, 0xffff0000, v1
	v_max_f32_e64 v3, |v3|, |v3|
	v_max_f32_e64 v7, |v7|, |v7|
	v_lshlrev_b32_e32 v6, 16, v2
	v_and_b32_e32 v2, 0xffff0000, v2
	v_max_f32_e64 v0, |v0|, |v0|
	v_max_f32_e64 v4, |v4|, |v4|
	v_max_f32_e64 v1, |v1|, |v1|
	v_max_f32_e64 v5, |v5|, |v5|
	v_max_f32_e32 v3, v7, v3
	v_max_f32_e32 v0, v4, v0
	v_max_f32_e32 v1, v5, v1
	v_max3_f32 v2, |v6|, |v2|, v3
	v_max3_f32 v0, v0, v1, v2
	v_max3_f32 v0, v10, 0, v0
	v_mov_b32_e32 v1, v0
	s_nop 1
	v_permlane16_swap_b32_e32 v0, v1
	v_max_f32_e32 v1, v1, v1
	v_max_f32_e32 v0, v0, v0
	v_max_f32_e32 v0, v0, v1
	v_mov_b32_e32 v1, v0
	s_nop 1
	v_permlane32_swap_b32_e32 v0, v1
	s_and_saveexec_b64 s[22:23], s[2:3]
	s_cbranch_execz .LBB0_761
	s_lshl_b64 s[20:21], s[20:21], 2
	s_add_u32 s20, s55, s20
	s_addc_u32 s21, s56, s21
	s_lshl_b32 s13, s13, 2
	s_add_u32 s20, s20, s13
	v_max_f32_e32 v0, v0, v0
	v_max_f32_e32 v1, v1, v1
	s_addc_u32 s21, s21, 0
	v_max_f32_e32 v2, v0, v1
	v_lshl_add_u64 v[0:1], v[136:137], 2, s[20:21]
	global_atomic_umax v[0:1], v2, off offset:704

.LBB0_777:
	s_ashr_i32 s18, s64, 3
	s_lshl_b32 s20, s18, 11
	s_ashr_i32 s21, s20, 31
	s_lshl_b64 s[20:21], s[20:21], 2
	v_lshl_or_b32 v154, s65, 8, v156
	s_add_u32 s20, s84, s20
	s_addc_u32 s21, s85, s21
	v_ashrrev_i32_e32 v155, 31, v154
	v_lshl_add_u64 v[152:153], v[154:155], 2, s[20:21]
	global_load_dwordx4 v[176:179], v[152:153], off
	global_load_dwordx4 v[180:183], v[152:153], off offset:16
	global_load_dwordx4 v[184:187], v[152:153], off offset:512
	global_load_dwordx4 v[188:191], v[152:153], off offset:528
	s_waitcnt vmcnt(0)
	s_nop 1
	v_mov_b64_e32 v[162:163], v[176:177]
	v_mov_b64_e32 v[164:165], v[178:179]
	s_nop 1
	v_mov_b64_e32 v[166:167], v[180:181]
	v_mov_b64_e32 v[168:169], v[182:183]
	s_ashr_i32 s19, s18, 31
	s_lshl_b32 s20, s64, 8
	s_lshl_b64 s[18:19], s[18:19], 11
	s_and_b32 s20, s20, 0x700
	s_or_b32 s18, s18, s20
	v_lshl_add_u64 v[170:171], s[18:19], 0, v[136:137]
	v_lshlrev_b64 v[170:171], 12, v[170:171]
	v_lshlrev_b64 v[154:155], 1, v[154:155]
	v_lshl_add_u64 v[170:171], s[6:7], 0, v[170:171]
	v_lshl_add_u64 v[170:171], v[170:171], 0, v[154:155]
	s_andn2_b64 vcc, exec, s[16:17]
	s_mov_b64 s[16:17], -1
	v_pk_mul_f32 v[124:125], v[124:125], v[162:163]
	v_pk_mul_f32 v[162:163], v[122:123], v[168:169]
	v_pk_mul_f32 v[122:123], v[120:121], v[166:167]
	v_pk_mul_f32 v[126:127], v[126:127], v[164:165]
	v_cvt_pk_bf16_f32 v120, v124, v125
	s_nop 0
	v_cvt_pk_bf16_f32 v121, v126, v127
	v_cvt_pk_bf16_f32 v122, v122, v123
	v_cvt_pk_bf16_f32 v123, v162, v163
	global_store_dwordx4 v[170:171], v[120:123], off
	s_nop 1
	v_mov_b64_e32 v[120:121], v[184:185]
	v_mov_b64_e32 v[122:123], v[186:187]
	s_nop 0
	s_nop 1
	v_mov_b64_e32 v[124:125], v[188:189]
	v_mov_b64_e32 v[126:127], v[190:191]
	v_pk_mul_f32 v[116:117], v[116:117], v[120:121]
	v_pk_mul_f32 v[120:121], v[114:115], v[126:127]
	v_pk_mul_f32 v[114:115], v[112:113], v[124:125]
	v_pk_mul_f32 v[118:119], v[118:119], v[122:123]
	v_cvt_pk_bf16_f32 v112, v116, v117
	s_nop 0
	v_cvt_pk_bf16_f32 v113, v118, v119
	v_cvt_pk_bf16_f32 v114, v114, v115
	v_cvt_pk_bf16_f32 v115, v120, v121
	global_store_dwordx4 v[170:171], v[112:115], off offset:256
	s_nop 1
	v_mov_b64_e32 v[112:113], v[176:177]
	v_mov_b64_e32 v[114:115], v[178:179]
	s_nop 1
	v_mov_b64_e32 v[116:117], v[180:181]
	v_mov_b64_e32 v[118:119], v[182:183]
	v_lshl_add_u64 v[120:121], s[18:19], 0, v[138:139]
	v_lshlrev_b64 v[120:121], 12, v[120:121]
	v_lshl_add_u64 v[120:121], s[6:7], 0, v[120:121]
	v_lshl_add_u64 v[120:121], v[120:121], 0, v[154:155]
	v_pk_mul_f32 v[108:109], v[108:109], v[112:113]
	v_pk_mul_f32 v[112:113], v[106:107], v[118:119]
	v_pk_mul_f32 v[106:107], v[104:105], v[116:117]
	v_pk_mul_f32 v[110:111], v[110:111], v[114:115]
	v_cvt_pk_bf16_f32 v104, v108, v109
	s_nop 0
	v_cvt_pk_bf16_f32 v105, v110, v111
	v_cvt_pk_bf16_f32 v106, v106, v107
	v_cvt_pk_bf16_f32 v107, v112, v113
	global_store_dwordx4 v[120:121], v[104:107], off
	s_nop 1
	v_mov_b64_e32 v[104:105], v[184:185]
	v_mov_b64_e32 v[106:107], v[186:187]
	s_nop 0
	s_nop 1
	v_mov_b64_e32 v[108:109], v[188:189]
	v_mov_b64_e32 v[110:111], v[190:191]
	v_pk_mul_f32 v[100:101], v[100:101], v[104:105]
	v_pk_mul_f32 v[104:105], v[98:99], v[110:111]
	v_pk_mul_f32 v[98:99], v[96:97], v[108:109]
	v_pk_mul_f32 v[102:103], v[102:103], v[106:107]
	v_cvt_pk_bf16_f32 v96, v100, v101
	s_nop 0
	v_cvt_pk_bf16_f32 v97, v102, v103
	v_cvt_pk_bf16_f32 v98, v98, v99
	v_cvt_pk_bf16_f32 v99, v104, v105
	global_store_dwordx4 v[120:121], v[96:99], off offset:256
	s_nop 1
	v_mov_b64_e32 v[96:97], v[176:177]
	v_mov_b64_e32 v[98:99], v[178:179]
	s_nop 1
	v_mov_b64_e32 v[100:101], v[180:181]
	v_mov_b64_e32 v[102:103], v[182:183]
	v_lshl_add_u64 v[104:105], s[18:19], 0, v[140:141]
	v_lshlrev_b64 v[104:105], 12, v[104:105]
	v_lshl_add_u64 v[104:105], s[6:7], 0, v[104:105]
	v_lshl_add_u64 v[104:105], v[104:105], 0, v[154:155]
	v_pk_mul_f32 v[92:93], v[92:93], v[96:97]
	v_pk_mul_f32 v[96:97], v[90:91], v[102:103]
	v_pk_mul_f32 v[90:91], v[88:89], v[100:101]
	v_pk_mul_f32 v[94:95], v[94:95], v[98:99]
	v_cvt_pk_bf16_f32 v88, v92, v93
	s_nop 0
	v_cvt_pk_bf16_f32 v89, v94, v95
	v_cvt_pk_bf16_f32 v90, v90, v91
	v_cvt_pk_bf16_f32 v91, v96, v97
	global_store_dwordx4 v[104:105], v[88:91], off
	s_nop 1
	v_mov_b64_e32 v[88:89], v[184:185]
	v_mov_b64_e32 v[90:91], v[186:187]
	s_nop 0
	s_nop 1
	v_mov_b64_e32 v[92:93], v[188:189]
	v_mov_b64_e32 v[94:95], v[190:191]
	v_pk_mul_f32 v[84:85], v[84:85], v[88:89]
	v_pk_mul_f32 v[88:89], v[82:83], v[94:95]
	v_pk_mul_f32 v[82:83], v[80:81], v[92:93]
	v_pk_mul_f32 v[86:87], v[86:87], v[90:91]
	v_cvt_pk_bf16_f32 v80, v84, v85
	s_nop 0
	v_cvt_pk_bf16_f32 v81, v86, v87
	v_cvt_pk_bf16_f32 v82, v82, v83
	v_cvt_pk_bf16_f32 v83, v88, v89
	global_store_dwordx4 v[104:105], v[80:83], off offset:256
	s_nop 1
	v_mov_b64_e32 v[80:81], v[176:177]
	v_mov_b64_e32 v[82:83], v[178:179]
	s_nop 1
	v_mov_b64_e32 v[84:85], v[180:181]
	v_mov_b64_e32 v[86:87], v[182:183]
	v_lshl_add_u64 v[88:89], s[18:19], 0, v[142:143]
	v_lshlrev_b64 v[88:89], 12, v[88:89]
	v_lshl_add_u64 v[88:89], s[6:7], 0, v[88:89]
	v_lshl_add_u64 v[88:89], v[88:89], 0, v[154:155]
	v_pk_mul_f32 v[76:77], v[76:77], v[80:81]
	v_pk_mul_f32 v[80:81], v[74:75], v[86:87]
	v_pk_mul_f32 v[74:75], v[72:73], v[84:85]
	v_pk_mul_f32 v[78:79], v[78:79], v[82:83]
	v_cvt_pk_bf16_f32 v72, v76, v77
	s_nop 0
	v_cvt_pk_bf16_f32 v73, v78, v79
	v_cvt_pk_bf16_f32 v74, v74, v75
	v_cvt_pk_bf16_f32 v75, v80, v81
	global_store_dwordx4 v[88:89], v[72:75], off
	s_nop 1
	v_mov_b64_e32 v[72:73], v[184:185]
	v_mov_b64_e32 v[74:75], v[186:187]
	s_nop 0
	s_nop 1
	v_mov_b64_e32 v[76:77], v[188:189]
	v_mov_b64_e32 v[78:79], v[190:191]
	v_pk_mul_f32 v[68:69], v[68:69], v[72:73]
	v_pk_mul_f32 v[72:73], v[66:67], v[78:79]
	v_pk_mul_f32 v[66:67], v[64:65], v[76:77]
	v_pk_mul_f32 v[70:71], v[70:71], v[74:75]
	v_cvt_pk_bf16_f32 v64, v68, v69
	s_nop 0
	v_cvt_pk_bf16_f32 v65, v70, v71
	v_cvt_pk_bf16_f32 v66, v66, v67
	v_cvt_pk_bf16_f32 v67, v72, v73
	global_store_dwordx4 v[88:89], v[64:67], off offset:256
	s_nop 1
	v_mov_b64_e32 v[64:65], v[176:177]
	v_mov_b64_e32 v[66:67], v[178:179]
	s_nop 1
	v_mov_b64_e32 v[68:69], v[180:181]
	v_mov_b64_e32 v[70:71], v[182:183]
	v_lshl_add_u64 v[72:73], s[18:19], 0, v[144:145]
	v_lshlrev_b64 v[72:73], 12, v[72:73]
	v_lshl_add_u64 v[72:73], s[6:7], 0, v[72:73]
	v_lshl_add_u64 v[72:73], v[72:73], 0, v[154:155]
	v_pk_mul_f32 v[60:61], v[60:61], v[64:65]
	v_pk_mul_f32 v[64:65], v[58:59], v[70:71]
	v_pk_mul_f32 v[58:59], v[56:57], v[68:69]
	v_pk_mul_f32 v[62:63], v[62:63], v[66:67]
	v_cvt_pk_bf16_f32 v56, v60, v61
	s_nop 0
	v_cvt_pk_bf16_f32 v57, v62, v63
	v_cvt_pk_bf16_f32 v58, v58, v59
	v_cvt_pk_bf16_f32 v59, v64, v65
	global_store_dwordx4 v[72:73], v[56:59], off
	s_nop 1
	v_mov_b64_e32 v[56:57], v[184:185]
	v_mov_b64_e32 v[58:59], v[186:187]
	s_nop 0
	s_nop 1
	v_mov_b64_e32 v[60:61], v[188:189]
	v_mov_b64_e32 v[62:63], v[190:191]
	v_pk_mul_f32 v[52:53], v[52:53], v[56:57]
	v_pk_mul_f32 v[56:57], v[50:51], v[62:63]
	v_pk_mul_f32 v[50:51], v[48:49], v[60:61]
	v_pk_mul_f32 v[54:55], v[54:55], v[58:59]
	v_cvt_pk_bf16_f32 v48, v52, v53
	s_nop 0
	v_cvt_pk_bf16_f32 v49, v54, v55
	v_cvt_pk_bf16_f32 v50, v50, v51
	v_cvt_pk_bf16_f32 v51, v56, v57
	global_store_dwordx4 v[72:73], v[48:51], off offset:256
	s_nop 1
	v_mov_b64_e32 v[48:49], v[176:177]
	v_mov_b64_e32 v[50:51], v[178:179]
	s_nop 1
	v_mov_b64_e32 v[52:53], v[180:181]
	v_mov_b64_e32 v[54:55], v[182:183]
	v_lshl_add_u64 v[56:57], s[18:19], 0, v[146:147]
	v_lshlrev_b64 v[56:57], 12, v[56:57]
	v_lshl_add_u64 v[56:57], s[6:7], 0, v[56:57]
	v_lshl_add_u64 v[56:57], v[56:57], 0, v[154:155]
	v_pk_mul_f32 v[44:45], v[44:45], v[48:49]
	v_pk_mul_f32 v[48:49], v[42:43], v[54:55]
	v_pk_mul_f32 v[42:43], v[40:41], v[52:53]
	v_pk_mul_f32 v[46:47], v[46:47], v[50:51]
	v_cvt_pk_bf16_f32 v40, v44, v45
	s_nop 0
	v_cvt_pk_bf16_f32 v41, v46, v47
	v_cvt_pk_bf16_f32 v42, v42, v43
	v_cvt_pk_bf16_f32 v43, v48, v49
	global_store_dwordx4 v[56:57], v[40:43], off
	s_nop 1
	v_mov_b64_e32 v[40:41], v[184:185]
	v_mov_b64_e32 v[42:43], v[186:187]
	s_nop 0
	s_nop 1
	v_mov_b64_e32 v[44:45], v[188:189]
	v_mov_b64_e32 v[46:47], v[190:191]
	v_pk_mul_f32 v[36:37], v[36:37], v[40:41]
	v_pk_mul_f32 v[40:41], v[34:35], v[46:47]
	v_pk_mul_f32 v[34:35], v[32:33], v[44:45]
	v_pk_mul_f32 v[38:39], v[38:39], v[42:43]
	v_cvt_pk_bf16_f32 v32, v36, v37
	s_nop 0
	v_cvt_pk_bf16_f32 v33, v38, v39
	v_cvt_pk_bf16_f32 v34, v34, v35
	v_cvt_pk_bf16_f32 v35, v40, v41
	global_store_dwordx4 v[56:57], v[32:35], off offset:256
	s_nop 1
	v_mov_b64_e32 v[32:33], v[176:177]
	v_mov_b64_e32 v[34:35], v[178:179]
	s_nop 1
	v_mov_b64_e32 v[36:37], v[180:181]
	v_mov_b64_e32 v[38:39], v[182:183]
	v_lshl_add_u64 v[40:41], s[18:19], 0, v[148:149]
	v_lshlrev_b64 v[40:41], 12, v[40:41]
	v_lshl_add_u64 v[40:41], s[6:7], 0, v[40:41]
	v_lshl_add_u64 v[40:41], v[40:41], 0, v[154:155]
	v_pk_mul_f32 v[28:29], v[28:29], v[32:33]
	v_pk_mul_f32 v[32:33], v[26:27], v[38:39]
	v_pk_mul_f32 v[26:27], v[24:25], v[36:37]
	v_pk_mul_f32 v[30:31], v[30:31], v[34:35]
	v_cvt_pk_bf16_f32 v24, v28, v29
	s_nop 0
	v_cvt_pk_bf16_f32 v25, v30, v31
	v_cvt_pk_bf16_f32 v26, v26, v27
	v_cvt_pk_bf16_f32 v27, v32, v33
	global_store_dwordx4 v[40:41], v[24:27], off
	s_nop 1
	v_mov_b64_e32 v[24:25], v[184:185]
	v_mov_b64_e32 v[26:27], v[186:187]
	s_nop 0
	s_nop 1
	v_mov_b64_e32 v[28:29], v[188:189]
	v_mov_b64_e32 v[30:31], v[190:191]
	v_pk_mul_f32 v[20:21], v[20:21], v[24:25]
	v_pk_mul_f32 v[24:25], v[18:19], v[30:31]
	v_pk_mul_f32 v[18:19], v[16:17], v[28:29]
	v_pk_mul_f32 v[22:23], v[22:23], v[26:27]
	v_cvt_pk_bf16_f32 v16, v20, v21
	s_nop 0
	v_cvt_pk_bf16_f32 v17, v22, v23
	v_cvt_pk_bf16_f32 v18, v18, v19
	v_cvt_pk_bf16_f32 v19, v24, v25
	global_store_dwordx4 v[40:41], v[16:19], off offset:256
	s_nop 1
	v_mov_b64_e32 v[16:17], v[176:177]
	v_mov_b64_e32 v[18:19], v[178:179]
	s_nop 1
	v_mov_b64_e32 v[20:21], v[180:181]
	v_mov_b64_e32 v[22:23], v[182:183]
	v_lshl_add_u64 v[24:25], s[18:19], 0, v[150:151]
	v_lshlrev_b64 v[24:25], 12, v[24:25]
	v_lshl_add_u64 v[24:25], s[6:7], 0, v[24:25]
	v_lshl_add_u64 v[24:25], v[24:25], 0, v[154:155]
	v_pk_mul_f32 v[12:13], v[12:13], v[16:17]
	v_pk_mul_f32 v[16:17], v[10:11], v[22:23]
	v_pk_mul_f32 v[10:11], v[8:9], v[20:21]
	v_pk_mul_f32 v[14:15], v[14:15], v[18:19]
	v_cvt_pk_bf16_f32 v8, v12, v13
	s_nop 0
	v_cvt_pk_bf16_f32 v9, v14, v15
	v_cvt_pk_bf16_f32 v10, v10, v11
	v_cvt_pk_bf16_f32 v11, v16, v17
	global_store_dwordx4 v[24:25], v[8:11], off
	s_nop 1
	v_mov_b64_e32 v[8:9], v[184:185]
	v_mov_b64_e32 v[10:11], v[186:187]
	s_nop 0
	s_nop 1
	v_mov_b64_e32 v[12:13], v[188:189]
	v_mov_b64_e32 v[14:15], v[190:191]
	v_pk_mul_f32 v[4:5], v[4:5], v[8:9]
	v_pk_mul_f32 v[8:9], v[2:3], v[14:15]
	v_pk_mul_f32 v[2:3], v[0:1], v[12:13]
	v_pk_mul_f32 v[6:7], v[6:7], v[10:11]
	v_cvt_pk_bf16_f32 v0, v4, v5
	s_nop 0
	v_cvt_pk_bf16_f32 v1, v6, v7
	v_cvt_pk_bf16_f32 v2, v2, v3
	v_cvt_pk_bf16_f32 v3, v8, v9
	global_store_dwordx4 v[24:25], v[0:3], off offset:256
	s_cbranch_vccnz .LBB0_770
	s_andn2_b64 vcc, exec, s[2:3]
	s_cbranch_vccnz .LBB0_769
	s_barrier
	s_branch .LBB0_769

.LBB0_1601:
	v_cndmask_b32_e64 v192, 0, 1, s[14:15]
	s_mov_b64 s[24:25], -1
	v_cmp_ne_u32_e64 s[6:7], 1, v192
	s_andn2_b64 vcc, exec, s[14:15]
	v_lshl_add_u64 v[222:223], v[218:219], 2, s[8:9]
	s_cbranch_vccnz .LBB0_1603
	v_lshlrev_b32_e32 v250, 2, v218
	global_load_dwordx4 v[188:191], v250, s[8:9]
	global_load_dwordx4 v[184:187], v250, s[8:9] offset:16
	global_load_dwordx4 v[180:183], v250, s[8:9] offset:512
	global_load_dwordx4 v[176:179], v250, s[8:9] offset:528
	s_add_u32 s44, s8, 0x20000
	s_addc_u32 s45, s9, 0
	global_load_dwordx4 v[172:175], v250, s[44:45]
	global_load_dwordx4 v[168:171], v250, s[44:45] offset:16
	s_add_u32 s44, s8, 0x20000
	s_addc_u32 s45, s9, 0
	global_load_dwordx4 v[164:167], v250, s[44:45] offset:512
	global_load_dwordx4 v[160:163], v250, s[44:45] offset:528
	s_add_u32 s44, s8, 0x40000
	s_addc_u32 s45, s9, 0
	global_load_dwordx4 v[148:151], v250, s[44:45]
	global_load_dwordx4 v[140:143], v250, s[44:45] offset:16
	s_add_u32 s44, s8, 0x40000
	s_addc_u32 s45, s9, 0
	global_load_dwordx4 v[128:131], v250, s[44:45] offset:512
	global_load_dwordx4 v[120:123], v250, s[44:45] offset:528
	s_add_u32 s44, s8, 0x60000
	s_addc_u32 s45, s9, 0
	global_load_dwordx4 v[108:111], v250, s[44:45]
	global_load_dwordx4 v[96:99], v250, s[44:45] offset:16
	s_add_u32 s44, s8, 0x60000
	s_addc_u32 s45, s9, 0
	global_load_dwordx4 v[88:91], v250, s[44:45] offset:512
	global_load_dwordx4 v[80:83], v250, s[44:45] offset:528
	s_add_u32 s44, s8, 0x160000
	s_addc_u32 s45, s9, 0
	global_load_dwordx4 v[244:247], v250, s[44:45] offset:512
	global_load_dwordx2 v[224:225], v250, s[44:45] offset:528
	global_load_dwordx2 v[248:249], v250, s[44:45] offset:536
	s_waitcnt vmcnt(17)
	v_mov_b64_e32 v[192:193], v[188:189]
	v_mov_b64_e32 v[194:195], v[190:191]
	v_mov_b64_e32 v[196:197], v[184:185]
	v_mov_b64_e32 v[198:199], v[186:187]
	s_mov_b64 s[24:25], 0

.LBB0_1605:
	v_pk_add_f32 v[190:191], v[158:159], v[194:195]
	v_pk_add_f32 v[194:195], v[156:157], v[192:193]
	v_pk_add_f32 v[188:189], v[154:155], v[198:199]
	v_pk_add_f32 v[192:193], v[152:153], v[196:197]
	v_cvt_pk_bf16_f32 v152, v194, v195
	v_cvt_pk_bf16_f32 v153, v190, v191
	s_and_b64 vcc, exec, s[6:7]
	v_cvt_pk_bf16_f32 v154, v192, v193
	v_cvt_pk_bf16_f32 v155, v188, v189
	s_mov_b64 s[24:25], -1
	global_store_dwordx4 v[220:221], v[152:155], off
	s_cbranch_vccnz .LBB0_1607
	s_waitcnt vmcnt(16)
	v_mov_b64_e32 v[152:153], v[180:181]
	v_mov_b64_e32 v[154:155], v[182:183]
	v_mov_b64_e32 v[156:157], v[176:177]
	v_mov_b64_e32 v[158:159], v[178:179]
	s_mov_b64 s[24:25], 0

.LBB0_1611:
	s_or_b64 exec, exec, s[26:27]
	s_mov_b64 s[0:1], 0x8000
	v_lshl_add_u64 v[156:157], v[218:219], 0, s[0:1]
	s_mov_b64 s[26:27], -1
	s_and_b64 vcc, exec, s[6:7]
	v_lshl_add_u64 v[152:153], v[156:157], 2, s[8:9]
	s_cbranch_vccnz .LBB0_1613
	s_waitcnt vmcnt(15)
	v_mov_b64_e32 v[136:137], v[172:173]
	v_mov_b64_e32 v[138:139], v[174:175]
	v_mov_b64_e32 v[144:145], v[168:169]
	v_mov_b64_e32 v[146:147], v[170:171]
	s_mov_b64 s[26:27], 0

.LBB0_1615:
	v_pk_add_f32 v[154:155], v[134:135], v[138:139]
	v_pk_add_f32 v[158:159], v[132:133], v[136:137]
	v_pk_add_f32 v[138:139], v[126:127], v[146:147]
	v_pk_add_f32 v[144:145], v[124:125], v[144:145]
	v_cvt_pk_bf16_f32 v124, v158, v159
	v_cvt_pk_bf16_f32 v125, v154, v155
	v_lshl_add_u64 v[136:137], v[156:157], 1, s[70:71]
	v_cvt_pk_bf16_f32 v126, v144, v145
	v_cvt_pk_bf16_f32 v127, v138, v139
	s_and_b64 vcc, exec, s[6:7]
	s_mov_b64 s[26:27], -1
	global_store_dwordx4 v[136:137], v[124:127], off
	s_cbranch_vccnz .LBB0_1617
	s_waitcnt vmcnt(14)
	v_mov_b64_e32 v[124:125], v[164:165]
	v_mov_b64_e32 v[126:127], v[166:167]
	v_mov_b64_e32 v[132:133], v[160:161]
	v_mov_b64_e32 v[134:135], v[162:163]
	s_mov_b64 s[26:27], 0

.LBB0_1621:
	s_or_b64 exec, exec, s[26:27]
	s_mov_b64 s[0:1], 0x10000
	v_lshl_add_u64 v[132:133], v[218:219], 0, s[0:1]
	s_mov_b64 s[26:27], -1
	s_and_b64 vcc, exec, s[6:7]
	v_lshl_add_u64 v[124:125], v[132:133], 2, s[8:9]
	s_cbranch_vccnz .LBB0_1623
	s_waitcnt vmcnt(13)
	v_mov_b64_e32 v[112:113], v[148:149]
	v_mov_b64_e32 v[114:115], v[150:151]
	v_mov_b64_e32 v[116:117], v[140:141]
	v_mov_b64_e32 v[118:119], v[142:143]
	s_add_u32 s44, s8, 0x100000
	s_addc_u32 s45, s9, 0
	global_load_dwordx4 v[148:151], v250, s[44:45]
	global_load_dwordx4 v[140:143], v250, s[44:45] offset:16
	s_mov_b64 s[26:27], 0

.LBB0_1625:
	v_pk_add_f32 v[126:127], v[106:107], v[114:115]
	v_pk_add_f32 v[134:135], v[104:105], v[112:113]
	v_pk_add_f32 v[114:115], v[102:103], v[118:119]
	v_pk_add_f32 v[116:117], v[100:101], v[116:117]
	v_cvt_pk_bf16_f32 v100, v134, v135
	v_cvt_pk_bf16_f32 v101, v126, v127
	v_lshl_add_u64 v[112:113], v[132:133], 1, s[70:71]
	v_cvt_pk_bf16_f32 v102, v116, v117
	v_cvt_pk_bf16_f32 v103, v114, v115
	s_and_b64 vcc, exec, s[6:7]
	s_mov_b64 s[26:27], -1
	global_store_dwordx4 v[112:113], v[100:103], off
	s_cbranch_vccnz .LBB0_1627
	s_waitcnt vmcnt(14)
	v_mov_b64_e32 v[100:101], v[128:129]
	v_mov_b64_e32 v[102:103], v[130:131]
	v_mov_b64_e32 v[104:105], v[120:121]
	v_mov_b64_e32 v[106:107], v[122:123]
	s_add_u32 s44, s8, 0x100000
	s_addc_u32 s45, s9, 0
	global_load_dwordx4 v[128:131], v250, s[44:45] offset:512
	global_load_dwordx4 v[120:123], v250, s[44:45] offset:528
	s_mov_b64 s[26:27], 0

.LBB0_1631:
	s_or_b64 exec, exec, s[26:27]
	s_mov_b64 s[0:1], 0x18000
	v_lshl_add_u64 v[104:105], v[218:219], 0, s[0:1]
	s_mov_b64 s[26:27], -1
	s_and_b64 vcc, exec, s[6:7]
	v_lshl_add_u64 v[100:101], v[104:105], 2, s[8:9]
	s_cbranch_vccnz .LBB0_1633
	s_waitcnt vmcnt(15)
	v_mov_b64_e32 v[84:85], v[108:109]
	v_mov_b64_e32 v[86:87], v[110:111]
	v_mov_b64_e32 v[92:93], v[96:97]
	v_mov_b64_e32 v[94:95], v[98:99]
	s_add_u32 s44, s8, 0x120000
	s_addc_u32 s45, s9, 0
	global_load_dwordx4 v[108:111], v250, s[44:45]
	global_load_dwordx4 v[96:99], v250, s[44:45] offset:16
	s_mov_b64 s[26:27], 0

.LBB0_1635:
	v_pk_add_f32 v[102:103], v[78:79], v[86:87]
	v_pk_add_f32 v[106:107], v[76:77], v[84:85]
	v_pk_add_f32 v[86:87], v[74:75], v[94:95]
	v_pk_add_f32 v[92:93], v[72:73], v[92:93]
	v_cvt_pk_bf16_f32 v72, v106, v107
	v_cvt_pk_bf16_f32 v73, v102, v103
	v_lshl_add_u64 v[84:85], v[104:105], 1, s[70:71]
	v_cvt_pk_bf16_f32 v74, v92, v93
	v_cvt_pk_bf16_f32 v75, v86, v87
	s_and_b64 vcc, exec, s[6:7]
	s_mov_b64 s[26:27], -1
	global_store_dwordx4 v[84:85], v[72:75], off
	s_cbranch_vccnz .LBB0_1637
	s_waitcnt vmcnt(16)
	v_mov_b64_e32 v[72:73], v[88:89]
	v_mov_b64_e32 v[74:75], v[90:91]
	v_mov_b64_e32 v[76:77], v[80:81]
	v_mov_b64_e32 v[78:79], v[82:83]
	s_add_u32 s44, s8, 0x120000
	s_addc_u32 s45, s9, 0
	global_load_dwordx4 v[88:91], v250, s[44:45] offset:512
	global_load_dwordx4 v[80:83], v250, s[44:45] offset:528
	s_mov_b64 s[26:27], 0

.LBB0_1641:
	s_or_b64 exec, exec, s[26:27]
	s_mov_b64 s[0:1], 0x40000
	v_lshl_add_u64 v[76:77], v[218:219], 0, s[0:1]
	s_mov_b64 s[26:27], -1
	s_and_b64 vcc, exec, s[6:7]
	v_lshl_add_u64 v[72:73], v[76:77], 2, s[8:9]
	s_cbranch_vccnz .LBB0_1643
	s_waitcnt vmcnt(10)
	v_mov_b64_e32 v[64:65], v[148:149]
	v_mov_b64_e32 v[66:67], v[150:151]
	v_mov_b64_e32 v[68:69], v[140:141]
	v_mov_b64_e32 v[70:71], v[142:143]
	s_mov_b64 s[26:27], 0

.LBB0_1645:
	v_pk_add_f32 v[74:75], v[62:63], v[66:67]
	v_pk_add_f32 v[78:79], v[60:61], v[64:65]
	v_pk_add_f32 v[66:67], v[58:59], v[70:71]
	v_pk_add_f32 v[68:69], v[56:57], v[68:69]
	v_cvt_pk_bf16_f32 v56, v78, v79
	v_cvt_pk_bf16_f32 v57, v74, v75
	v_lshl_add_u64 v[64:65], v[76:77], 1, s[70:71]
	v_cvt_pk_bf16_f32 v58, v68, v69
	v_cvt_pk_bf16_f32 v59, v66, v67
	s_and_b64 vcc, exec, s[6:7]
	s_mov_b64 s[26:27], -1
	global_store_dwordx4 v[64:65], v[56:59], off
	s_cbranch_vccnz .LBB0_1647
	s_waitcnt vmcnt(8)
	v_mov_b64_e32 v[56:57], v[128:129]
	v_mov_b64_e32 v[58:59], v[130:131]
	v_mov_b64_e32 v[60:61], v[120:121]
	v_mov_b64_e32 v[62:63], v[122:123]
	s_mov_b64 s[26:27], 0

.LBB0_1651:
	s_or_b64 exec, exec, s[26:27]
	s_mov_b64 s[0:1], 0x48000
	v_lshl_add_u64 v[60:61], v[218:219], 0, s[0:1]
	s_mov_b64 s[26:27], -1
	s_and_b64 vcc, exec, s[6:7]
	v_lshl_add_u64 v[56:57], v[60:61], 2, s[8:9]
	s_cbranch_vccnz .LBB0_1653
	s_waitcnt vmcnt(6)
	v_mov_b64_e32 v[48:49], v[108:109]
	v_mov_b64_e32 v[50:51], v[110:111]
	v_mov_b64_e32 v[52:53], v[96:97]
	v_mov_b64_e32 v[54:55], v[98:99]
	s_add_u32 s44, s8, 0x140000
	s_addc_u32 s45, s9, 0
	global_load_dwordx4 v[108:111], v250, s[44:45]
	global_load_dwordx4 v[96:99], v250, s[44:45] offset:16
	s_mov_b64 s[26:27], 0

.LBB0_1655:
	v_pk_add_f32 v[58:59], v[46:47], v[50:51]
	v_pk_add_f32 v[62:63], v[44:45], v[48:49]
	v_pk_add_f32 v[50:51], v[42:43], v[54:55]
	v_pk_add_f32 v[52:53], v[40:41], v[52:53]
	v_cvt_pk_bf16_f32 v40, v62, v63
	v_cvt_pk_bf16_f32 v41, v58, v59
	v_lshl_add_u64 v[48:49], v[60:61], 1, s[70:71]
	v_cvt_pk_bf16_f32 v42, v52, v53
	v_cvt_pk_bf16_f32 v43, v50, v51
	s_and_b64 vcc, exec, s[6:7]
	s_mov_b64 s[26:27], -1
	global_store_dwordx4 v[48:49], v[40:43], off
	s_cbranch_vccnz .LBB0_1657
	s_waitcnt vmcnt(6)
	v_mov_b64_e32 v[40:41], v[88:89]
	v_mov_b64_e32 v[42:43], v[90:91]
	v_mov_b64_e32 v[44:45], v[80:81]
	v_mov_b64_e32 v[46:47], v[82:83]
	s_add_u32 s44, s8, 0x140000
	s_addc_u32 s45, s9, 0
	global_load_dwordx4 v[88:91], v250, s[44:45] offset:512
	global_load_dwordx4 v[80:83], v250, s[44:45] offset:528
	s_mov_b64 s[26:27], 0

.LBB0_1661:
	s_or_b64 exec, exec, s[26:27]
	s_mov_b64 s[0:1], 0x50000
	v_lshl_add_u64 v[44:45], v[218:219], 0, s[0:1]
	s_mov_b64 s[26:27], -1
	s_and_b64 vcc, exec, s[6:7]
	v_lshl_add_u64 v[40:41], v[44:45], 2, s[8:9]
	s_cbranch_vccnz .LBB0_1663
	s_waitcnt vmcnt(4)
	v_mov_b64_e32 v[32:33], v[108:109]
	v_mov_b64_e32 v[34:35], v[110:111]
	v_mov_b64_e32 v[36:37], v[96:97]
	v_mov_b64_e32 v[38:39], v[98:99]
	s_mov_b64 s[26:27], 0

.LBB0_1665:
	v_pk_add_f32 v[42:43], v[30:31], v[34:35]
	v_pk_add_f32 v[46:47], v[28:29], v[32:33]
	v_pk_add_f32 v[34:35], v[26:27], v[38:39]
	v_pk_add_f32 v[36:37], v[24:25], v[36:37]
	v_cvt_pk_bf16_f32 v24, v46, v47
	v_cvt_pk_bf16_f32 v25, v42, v43
	v_lshl_add_u64 v[32:33], v[44:45], 1, s[70:71]
	v_cvt_pk_bf16_f32 v26, v36, v37
	v_cvt_pk_bf16_f32 v27, v34, v35
	s_and_b64 vcc, exec, s[6:7]
	s_mov_b64 s[26:27], -1
	global_store_dwordx4 v[32:33], v[24:27], off
	s_cbranch_vccnz .LBB0_1667
	s_waitcnt vmcnt(2)
	v_mov_b64_e32 v[24:25], v[88:89]
	v_mov_b64_e32 v[26:27], v[90:91]
	v_mov_b64_e32 v[28:29], v[80:81]
	v_mov_b64_e32 v[30:31], v[82:83]
	s_add_u32 s44, s8, 0x160000
	s_addc_u32 s45, s9, 0
	global_load_dwordx4 v[88:91], v250, s[44:45]
	global_load_dwordx4 v[80:83], v250, s[44:45] offset:16
	s_mov_b64 s[26:27], 0

.LBB0_1671:
	s_or_b64 exec, exec, s[26:27]
	s_mov_b64 s[0:1], 0x58000
	v_lshl_add_u64 v[28:29], v[218:219], 0, s[0:1]
	s_mov_b64 s[26:27], -1
	s_and_b64 vcc, exec, s[6:7]
	v_lshl_add_u64 v[24:25], v[28:29], 2, s[8:9]
	s_cbranch_vccnz .LBB0_1673
	s_waitcnt vmcnt(1)
	v_mov_b64_e32 v[16:17], v[88:89]
	v_mov_b64_e32 v[18:19], v[90:91]
	v_mov_b64_e32 v[20:21], v[80:81]
	v_mov_b64_e32 v[22:23], v[82:83]
	s_mov_b64 s[26:27], 0

.LBB0_1675:
	v_pk_add_f32 v[26:27], v[14:15], v[18:19]
	v_pk_add_f32 v[30:31], v[12:13], v[16:17]
	v_pk_add_f32 v[18:19], v[10:11], v[22:23]
	v_pk_add_f32 v[20:21], v[8:9], v[20:21]
	v_cvt_pk_bf16_f32 v8, v30, v31
	v_cvt_pk_bf16_f32 v9, v26, v27
	v_lshl_add_u64 v[16:17], v[28:29], 1, s[70:71]
	v_cvt_pk_bf16_f32 v10, v20, v21
	v_cvt_pk_bf16_f32 v11, v18, v19
	s_and_b64 vcc, exec, s[6:7]
	s_mov_b64 s[6:7], -1
	global_store_dwordx4 v[16:17], v[8:11], off
	s_cbranch_vccnz .LBB0_1677
	s_waitcnt vmcnt(29)
	v_mov_b64_e32 v[8:9], v[244:245]
	v_mov_b64_e32 v[10:11], v[246:247]
	v_mov_b64_e32 v[12:13], v[224:225]
	v_mov_b64_e32 v[14:15], v[248:249]
	s_mov_b64 s[6:7], 0
